# speedup vs baseline: 1.0499x; 1.0006x over previous
_Z11lstm_kernelPKiPKhPKfS4_S4_Pf:
	s_load_dwordx4 s[12:15], s[0:1], 0x0
	v_readfirstlane_b32 s19, v0
	v_or_b32_e32 v3, 0x400, v0
	s_movk_i32 s4, 0x500
	s_lshr_b32 s7, s19, 6
	s_lshl_b32 s18, s2, 6
	s_mulk_i32 s2, 0x1400
	v_mov_b32_e32 v2, 0x4ff
	v_cmp_gt_u32_e32 vcc, s4, v3
	s_mul_hi_i32 s3, s18, 0x50
	s_waitcnt lgkmcnt(0)
	s_add_u32 s2, s12, s2
	v_cndmask_b32_e32 v2, v2, v3, vcc
	s_addc_u32 s3, s13, s3
	v_lshlrev_b32_e32 v1, 2, v0
	v_lshlrev_b32_e32 v4, 2, v2
	s_movk_i32 s4, 0x184
	v_or_b32_e32 v28, 0x200, v0
	global_load_dword v29, v1, s[2:3]
	global_load_dword v30, v1, s[2:3] offset:2048
	global_load_dword v2, v4, s[2:3]
	v_mov_b32_e32 v4, 0x383
	v_cmp_gt_u32_e32 vcc, s4, v0
	s_add_u32 s2, s14, 0x34000
	s_addc_u32 s3, s15, 0
	v_cndmask_b32_e32 v4, v4, v28, vcc
	v_lshlrev_b32_e32 v31, 4, v0
	v_lshlrev_b32_e32 v4, 4, v4
	global_load_dwordx4 v[6:9], v31, s[2:3]
	global_load_dwordx4 v[10:13], v4, s[2:3]
	v_and_b32_e32 v4, 0x7f, v0
	v_lshlrev_b32_e32 v18, 4, v4
	v_mov_b32_e32 v19, 0
	v_lshl_add_u64 v[4:5], s[14:15], 0, v[18:19]
	s_mov_b32 s2, 0x37000
	v_add_co_u32_e64 v4, s[2:3], s2, v4
	s_nop 1
	v_addc_co_u32_e64 v5, s[2:3], 0, v5, s[2:3]
	global_load_dwordx4 v[14:17], v[4:5], off offset:2112
	s_movk_i32 s22, 0x410
	s_movk_i32 s2, 0x4ff
	v_and_b32_e32 v4, 63, v0
	v_cmp_lt_u32_e64 s[2:3], s2, v3
	s_mul_i32 s5, s7, 0x6000
	s_mul_hi_u32 s4, s7, 0x6000
	s_add_u32 s8, s14, s5
	s_addc_u32 s9, s15, s4
	v_lshlrev_b32_e32 v210, 4, v4
	v_mov_b32_e32 v211, v19
	v_lshl_add_u64 v[20:21], s[8:9], 0, v[210:211]
	s_movk_i32 s4, 0x2000
	v_add_co_u32_e64 v22, s[4:5], s4, v20
	s_nop 1
	v_addc_co_u32_e64 v23, s[4:5], 0, v21, s[4:5]
	s_movk_i32 s4, 0x3000
	s_nop 0
	v_add_co_u32_e64 v24, s[4:5], s4, v20
	global_load_dwordx4 v[90:93], v[22:23], off offset:1024
	global_load_dwordx4 v[86:89], v[22:23], off offset:2048
	v_addc_co_u32_e64 v25, s[4:5], 0, v21, s[4:5]
	s_movk_i32 s4, 0x5000
	s_nop 0
	v_add_co_u32_e64 v26, s[4:5], s4, v20
	s_nop 1
	v_addc_co_u32_e64 v27, s[4:5], 0, v21, s[4:5]
	global_load_dwordx4 v[82:85], v[22:23], off offset:3072
	global_load_dwordx4 v[46:49], v[26:27], off
	global_load_dwordx4 v[42:45], v[26:27], off offset:1024
	global_load_dwordx4 v[38:41], v[26:27], off offset:2048
	global_load_dwordx4 v[94:97], v[24:25], off offset:-4096
	global_load_dwordx4 v[34:37], v[26:27], off offset:3072
	s_movk_i32 s4, 0x1000
	v_add_co_u32_e64 v22, s[4:5], s4, v20
	global_load_dwordx4 v[126:129], v210, s[8:9]
	global_load_dwordx4 v[122:125], v210, s[8:9] offset:1024
	global_load_dwordx4 v[118:121], v210, s[8:9] offset:2048
	global_load_dwordx4 v[114:117], v210, s[8:9] offset:3072
	v_addc_co_u32_e64 v23, s[4:5], 0, v21, s[4:5]
	global_load_dwordx4 v[110:113], v[22:23], off
	global_load_dwordx4 v[106:109], v[22:23], off offset:1024
	global_load_dwordx4 v[102:105], v[22:23], off offset:2048
	global_load_dwordx4 v[98:101], v[22:23], off offset:3072
	global_load_dwordx4 v[78:81], v[24:25], off
	global_load_dwordx4 v[74:77], v[24:25], off offset:1024
	global_load_dwordx4 v[70:73], v[24:25], off offset:2048
	global_load_dwordx4 v[66:69], v[24:25], off offset:3072
	s_movk_i32 s4, 0x4000
	v_add_co_u32_e64 v20, s[4:5], s4, v20
	v_mov_b32_e32 v5, 0x4000
	s_nop 0
	v_addc_co_u32_e64 v21, s[4:5], 0, v21, s[4:5]
	global_load_dwordx4 v[62:65], v[20:21], off
	global_load_dwordx4 v[58:61], v[20:21], off offset:1024
	global_load_dwordx4 v[54:57], v[20:21], off offset:2048
	global_load_dwordx4 v[50:53], v[20:21], off offset:3072
	s_waitcnt vmcnt(26)
	ds_write_b128 v31, v[6:9] offset:16384
	v_lshl_or_b32 v5, v28, 4, v5
	v_add_u32_e32 v6, 0x9840, v31
	v_cndmask_b32_e32 v5, v6, v5, vcc
	s_waitcnt vmcnt(25)
	ds_write_b128 v5, v[10:13]
	s_waitcnt vmcnt(24)
	ds_write_b128 v18, v[14:17] offset:36928
	v_mul_u32_u24_e32 v5, 0xccd, v0
	v_lshrrev_b32_e32 v5, 16, v5
	s_mov_b32 s5, 0xffffec
	v_mul_u32_u24_e32 v6, 0xccd, v28
	s_movk_i32 s4, 0x90
	v_mad_u32_u24 v8, v5, s5, v0
	v_lshlrev_b32_e32 v5, 2, v5
	v_lshrrev_b32_e32 v6, 16, v6
	v_mul_lo_u32 v7, v29, s4
	v_lshl_or_b32 v5, v8, 8, v5
	ds_write_b32 v5, v7 offset:30784
	v_mul_lo_u32 v196, v29, s22
	v_add_u32_e32 v197, 0x24e80, v5
	ds_write_b32 v197, v196
	v_mad_u32_u24 v7, v6, s5, v28
	v_lshlrev_b32_e32 v6, 2, v6
	v_mul_lo_u32 v5, v30, s4
	v_lshl_or_b32 v6, v7, 8, v6
	ds_write_b32 v6, v5 offset:30784
	v_mul_lo_u32 v198, v30, s22
	v_add_u32_e32 v199, 0x24e80, v6
	ds_write_b32 v199, v198
	s_and_saveexec_b64 s[4:5], s[2:3]
	s_xor_b64 s[2:3], exec, s[4:5]
	v_mov_b32_e32 v3, 0x9840
	v_lshl_add_u32 v5, v0, 2, v3
	s_andn2_saveexec_b64 s[2:3], s[2:3]
	v_mul_u32_u24_e32 v5, 0xccd, v3
	s_mov_b32 s4, 0xffffec
	v_mul_u32_u24_sdwa v6, v5, s4 dst_sel:DWORD dst_unused:UNUSED_PAD src0_sel:WORD_1 src1_sel:DWORD
	v_add_lshl_u32 v3, v6, v3, 8
	v_mov_b32_e32 v6, 2
	v_lshlrev_b32_sdwa v5, v6, v5 dst_sel:DWORD dst_unused:UNUSED_PAD src0_sel:DWORD src1_sel:WORD_1
	s_movk_i32 s4, 0x7840
	v_add3_u32 v5, v5, v3, s4
	s_or_b64 exec, exec, s[2:3]
	v_lshrrev_b32_e32 v3, 5, v4
	s_movk_i32 s2, 0x90
	s_lshl_b32 s6, s7, 10
	s_mulk_i32 s7, 0xfd00
	v_and_b32_e32 v182, 31, v0
	v_mul_lo_u32 v200, v2, s22
	v_mul_lo_u32 v2, v2, s2
	s_add_i32 s7, s6, s7
	v_lshlrev_b32_e32 v229, 6, v3
	ds_write_b32 v5, v2
	v_add_u32_e32 v201, 0x1d640, v5
	ds_write_b32 v201, v200
	v_lshlrev_b32_e32 v230, 4, v3
	v_lshlrev_b32_e32 v228, 2, v182
	v_or_b32_e32 v2, s7, v229
	s_waitcnt lgkmcnt(0)
	s_barrier
	s_cmpk_lt_u32 s19, 0x100
	s_cbranch_scc0 .Llight_path
	s_setprio 1
	v_add_u32_e32 v3, 0x7800, v228
	ds_read2_b32 v[138:139], v3 offset0:16 offset1:48
	ds_read_b128 v[18:21], v2 offset:36928
	ds_read_b128 v[22:25], v2 offset:36944
	s_waitcnt lgkmcnt(2)
	v_add_u32_e32 v3, v230, v138
	ds_read_b128 v[26:29], v2 offset:36960
	ds_read_b128 v[30:33], v2 offset:36976
	ds_read_b128 v[142:145], v3 offset:16384
	ds_read_b128 v[130:133], v3 offset:16416
	ds_read_b128 v[154:157], v3 offset:16448
	ds_read_b128 v[134:137], v3 offset:16480
	ds_read_b128 v[248:251], v2 offset:37104
	ds_read_b128 v[244:247], v2 offset:37088
	ds_read_b128 v[240:243], v2 offset:37072
	ds_read_b128 v[236:239], v2 offset:37056
	s_waitcnt vmcnt(17) lgkmcnt(7)
	v_mfma_f32_32x32x16_bf16 v[18:33], v[94:97], v[142:145], v[18:33]
	s_waitcnt lgkmcnt(6)
	v_mfma_f32_32x32x16_bf16 v[18:33], v[90:93], v[130:133], v[18:33]
	s_waitcnt lgkmcnt(5)
	v_mfma_f32_32x32x16_bf16 v[18:33], v[86:89], v[154:157], v[18:33]
	s_waitcnt lgkmcnt(4)
	v_mfma_f32_32x32x16_bf16 v[18:33], v[82:85], v[134:137], v[18:33]
	s_cmpk_lt_u32 s19, 0x100
	s_cselect_b64 s[2:3], -1, 0
	ds_read_b32 v158, v228 offset:31040
	v_add_u32_e32 v159, v230, v139
	s_nop 2
	v_exp_f32_e32 v139, v20
	v_exp_f32_e32 v138, v24
	v_exp_f32_e32 v141, v28
	v_exp_f32_e32 v140, v32
	v_exp_f32_e32 v18, v18
	v_exp_f32_e32 v20, v22
	v_exp_f32_e32 v22, v26
	v_add_f32_e32 v24, 1.0, v138
	v_add_f32_e32 v26, 1.0, v141
	v_add_f32_e32 v19, 1.0, v139
	v_exp_f32_e32 v23, v30
	v_add_f32_e32 v27, 1.0, v140
	v_fmac_f32_e32 v24, v20, v24
	v_fmac_f32_e32 v26, v22, v26
	v_fmac_f32_e32 v19, v18, v19
	v_fmac_f32_e32 v27, v23, v27
	v_rcp_f32_e32 v18, v24
	v_rcp_f32_e32 v22, v27
	v_rcp_f32_e32 v19, v19
	v_rcp_f32_e32 v23, v26
	v_exp_f32_e32 v146, v21
	v_exp_f32_e32 v147, v25
	s_mov_b32 s8, 0xc038aa3b
	s_mov_b32 s4, 0x4038aa3b
	v_mov_b64_e32 v[160:161], s[8:9]
	v_exp_f32_e32 v148, v29
	v_exp_f32_e32 v149, v33
	v_pk_fma_f32 v[20:21], v[138:139], s[4:5], v[160:161] op_sel_hi:[1,0,0]
	s_nop 0
	v_pk_mul_f32 v[214:215], v[20:21], v[18:19]
	v_pk_fma_f32 v[18:19], v[140:141], s[4:5], v[160:161] op_sel_hi:[1,0,0]
	s_nop 0
	v_pk_mul_f32 v[212:213], v[18:19], v[22:23]
	v_add_u32_e32 v231, s7, v229
	ds_read_b128 v[18:21], v231 offset:36928
	ds_read_b128 v[22:25], v231 offset:36944
	ds_read_b128 v[26:29], v231 offset:36960
	ds_read_b128 v[30:33], v231 offset:36976
	s_waitcnt lgkmcnt(5)
	v_mfma_f32_32x32x16_bf16 v[2:17], v[46:49], v[142:145], v[236:251]
	ds_read_b128 v[138:141], v159 offset:16384
	v_add_f32_e32 v162, 1.0, v146
	v_exp_f32_e32 v163, v215
	v_exp_f32_e32 v164, v214
	v_exp_f32_e32 v165, v213
	v_exp_f32_e32 v166, v212
	v_add_f32_e32 v142, 1.0, v147
	v_add_f32_e32 v143, 1.0, v148
	v_add_f32_e32 v144, 1.0, v149
	v_mfma_f32_32x32x16_bf16 v[2:17], v[42:45], v[130:133], v[2:17]
	ds_read_b128 v[146:149], v159 offset:16416
	v_fmac_f32_e32 v162, v162, v163
	v_fmac_f32_e32 v142, v142, v164
	v_fmac_f32_e32 v143, v143, v165
	v_fmac_f32_e32 v144, v144, v166
	v_mfma_f32_32x32x16_bf16 v[2:17], v[38:41], v[154:157], v[2:17]
	ds_read_b128 v[150:153], v159 offset:16448
	v_rcp_f32_e32 v130, v162
	v_rcp_f32_e32 v131, v142
	v_rcp_f32_e32 v132, v143
	v_rcp_f32_e32 v133, v144
	s_waitcnt vmcnt(16)
	v_mfma_f32_32x32x16_bf16 v[2:17], v[34:37], v[134:137], v[2:17]
	ds_read_b128 v[178:181], v159 offset:16480
	v_fma_f32 v130, -v163, v130, v130
	v_fma_f32 v131, -v164, v131, v131
	v_fma_f32 v132, -v165, v132, v132
	v_fma_f32 v133, -v166, v133, v133
	v_add_u32_e32 v211, s6, v210
	v_cvt_pk_bf16_f32 v130, v130, v131
	v_cvt_pk_bf16_f32 v131, v132, v133
	ds_write_b64 v211, v[130:131]
	s_nop 3
	v_exp_f32_e32 v131, v4
	v_exp_f32_e32 v130, v8
	v_exp_f32_e32 v133, v12
	v_exp_f32_e32 v132, v16
	v_exp_f32_e32 v2, v2
	v_exp_f32_e32 v4, v6
	v_exp_f32_e32 v6, v10
	v_exp_f32_e32 v7, v14
	v_add_f32_e32 v3, 1.0, v131
	v_add_f32_e32 v8, 1.0, v130
	v_add_f32_e32 v10, 1.0, v133
	v_add_f32_e32 v11, 1.0, v132
	v_fmac_f32_e32 v3, v2, v3
	v_fmac_f32_e32 v8, v4, v8
	v_fmac_f32_e32 v10, v6, v10
	v_fmac_f32_e32 v11, v7, v11
	v_rcp_f32_e32 v3, v3
	v_rcp_f32_e32 v2, v8
	v_rcp_f32_e32 v7, v10
	v_rcp_f32_e32 v6, v11
	v_exp_f32_e32 v134, v5
	v_exp_f32_e32 v135, v9
	v_pk_fma_f32 v[4:5], v[130:131], s[4:5], v[160:161] op_sel_hi:[1,0,0]
	v_exp_f32_e32 v130, v13
	v_pk_mul_f32 v[204:205], v[4:5], v[2:3]
	v_pk_fma_f32 v[2:3], v[132:133], s[4:5], v[160:161] op_sel_hi:[1,0,0]
	v_exp_f32_e32 v131, v17
	v_pk_mul_f32 v[202:203], v[2:3], v[6:7]
	s_waitcnt lgkmcnt(4)
	v_mfma_f32_32x32x16_bf16 v[18:33], v[94:97], v[138:141], v[18:33]
	v_add_f32_e32 v132, 1.0, v134
	v_exp_f32_e32 v133, v205
	v_add_f32_e32 v134, 1.0, v135
	v_exp_f32_e32 v135, v204
	v_exp_f32_e32 v136, v203
	v_exp_f32_e32 v137, v202
	v_add_f32_e32 v130, 1.0, v130
	v_add_f32_e32 v131, 1.0, v131
	s_waitcnt lgkmcnt(3)
	v_mfma_f32_32x32x16_bf16 v[18:33], v[90:93], v[146:149], v[18:33]
	v_fmac_f32_e32 v132, v132, v133
	v_fmac_f32_e32 v134, v134, v135
	v_fmac_f32_e32 v130, v130, v136
	v_fmac_f32_e32 v131, v131, v137
	s_waitcnt lgkmcnt(2)
	v_mfma_f32_32x32x16_bf16 v[18:33], v[86:89], v[150:153], v[18:33]
	v_rcp_f32_e32 v132, v132
	v_rcp_f32_e32 v134, v134
	v_rcp_f32_e32 v130, v130
	v_rcp_f32_e32 v131, v131
	s_waitcnt lgkmcnt(1)
	v_mfma_f32_32x32x16_bf16 v[18:33], v[82:85], v[178:181], v[18:33]
	v_fma_f32 v132, -v133, v132, v132
	v_fma_f32 v133, -v135, v134, v134
	v_fma_f32 v134, -v136, v130, v130
	v_fma_f32 v131, -v137, v131, v131
	v_cvt_pk_bf16_f32 v130, v132, v133
	v_cvt_pk_bf16_f32 v131, v134, v131
	ds_write_b64 v211, v[130:131] offset:8
	s_waitcnt lgkmcnt(0)
	s_barrier
	s_load_dwordx8 s[4:11], s[0:1], 0x10
	ds_read_b32 v194, v228 offset:31168
	ds_read_b128 v[174:177], v210
	v_add_u32_e32 v183, v230, v158
	ds_read_b128 v[170:173], v210 offset:1024
	v_exp_f32_e32 v131, v20
	v_exp_f32_e32 v130, v24
	v_exp_f32_e32 v133, v28
	v_exp_f32_e32 v132, v32
	ds_read_b128 v[166:169], v210 offset:2048
	v_exp_f32_e32 v18, v18
	v_exp_f32_e32 v20, v22
	v_exp_f32_e32 v22, v26
	v_exp_f32_e32 v23, v30
	v_add_f32_e32 v19, 1.0, v131
	v_add_f32_e32 v24, 1.0, v130
	v_add_f32_e32 v26, 1.0, v133
	v_add_f32_e32 v27, 1.0, v132
	ds_read_b128 v[162:165], v210 offset:3072
	v_fmac_f32_e32 v19, v18, v19
	v_fmac_f32_e32 v24, v20, v24
	v_fmac_f32_e32 v26, v22, v26
	v_fmac_f32_e32 v27, v23, v27
	ds_read_b128 v[158:161], v210 offset:4096
	v_rcp_f32_e32 v19, v19
	v_rcp_f32_e32 v18, v24
	v_rcp_f32_e32 v23, v26
	v_rcp_f32_e32 v22, v27
	ds_read_b128 v[154:157], v210 offset:5120
	v_exp_f32_e32 v186, v21
	v_exp_f32_e32 v187, v25
	ds_read_b128 v[142:145], v210 offset:6144
	s_mov_b32 s0, 0xc038aa3b
	s_mov_b32 s12, 0x4038aa3b
	v_mov_b64_e32 v[184:185], s[0:1]
	v_pk_fma_f32 v[20:21], v[130:131], s[12:13], v[184:185] op_sel_hi:[1,0,0]
	v_exp_f32_e32 v188, v29
	v_pk_mul_f32 v[200:201], v[20:21], v[18:19]
	v_pk_fma_f32 v[18:19], v[132:133], s[12:13], v[184:185] op_sel_hi:[1,0,0]
	v_exp_f32_e32 v189, v33
	v_pk_mul_f32 v[198:199], v[18:19], v[22:23]
	ds_read_b128 v[130:133], v210 offset:7168
	ds_read_b128 v[18:21], v231 offset:36928
	ds_read_b128 v[22:25], v231 offset:36944
	ds_read_b128 v[26:29], v231 offset:36960
	ds_read_b128 v[30:33], v231 offset:36976
	v_mfma_f32_32x32x16_bf16 v[2:17], v[46:49], v[138:141], v[236:251]
	ds_read_b128 v[134:137], v183 offset:16384
	v_add_f32_e32 v186, 1.0, v186
	v_exp_f32_e32 v190, v201
	v_exp_f32_e32 v191, v200
	v_exp_f32_e32 v192, v199
	v_exp_f32_e32 v193, v198
	v_add_f32_e32 v187, 1.0, v187
	v_add_f32_e32 v188, 1.0, v188
	v_add_f32_e32 v189, 1.0, v189
	v_mfma_f32_32x32x16_bf16 v[2:17], v[42:45], v[146:149], v[2:17]
	ds_read_b128 v[138:141], v183 offset:16416
	v_fmac_f32_e32 v186, v186, v190
	v_fmac_f32_e32 v187, v187, v191
	v_fmac_f32_e32 v188, v188, v192
	v_fmac_f32_e32 v189, v189, v193
	v_mfma_f32_32x32x16_bf16 v[2:17], v[38:41], v[150:153], v[2:17]
	ds_read_b128 v[146:149], v183 offset:16448
	v_rcp_f32_e32 v186, v186
	v_rcp_f32_e32 v187, v187
	v_rcp_f32_e32 v188, v188
	v_rcp_f32_e32 v189, v189
	v_mfma_f32_32x32x16_bf16 v[2:17], v[34:37], v[178:181], v[2:17]
	ds_read_b128 v[150:153], v183 offset:16480
	v_fma_f32 v183, -v190, v186, v186
	v_fma_f32 v186, -v191, v187, v187
	v_fma_f32 v187, -v192, v188, v188
	v_fma_f32 v188, -v193, v189, v189
	s_waitcnt vmcnt(15) lgkmcnt(0)
	v_mfma_f32_32x32x16_bf16 v[18:33], v[126:129], v[174:177], v[18:33]
	v_cvt_pk_bf16_f32 v178, v183, v186
	v_cvt_pk_bf16_f32 v179, v187, v188
	ds_write_b64 v211, v[178:179] offset:8192
	s_waitcnt vmcnt(14)
	v_mfma_f32_32x32x16_bf16 v[18:33], v[122:125], v[170:173], v[18:33]
	s_nop 0
	v_exp_f32_e32 v179, v4
	v_exp_f32_e32 v178, v8
	v_exp_f32_e32 v181, v12
	v_exp_f32_e32 v180, v16
	s_waitcnt vmcnt(13)
	v_mfma_f32_32x32x16_bf16 v[18:33], v[118:121], v[166:169], v[18:33]
	v_exp_f32_e32 v2, v2
	v_exp_f32_e32 v4, v6
	v_exp_f32_e32 v7, v10
	v_exp_f32_e32 v8, v14
	v_add_f32_e32 v3, 1.0, v179
	v_add_f32_e32 v6, 1.0, v178
	v_add_f32_e32 v10, 1.0, v181
	v_add_f32_e32 v11, 1.0, v180
	s_waitcnt vmcnt(12)
	v_mfma_f32_32x32x16_bf16 v[18:33], v[114:117], v[162:165], v[18:33]
	v_fmac_f32_e32 v3, v2, v3
	v_fmac_f32_e32 v6, v4, v6
	v_fmac_f32_e32 v10, v7, v10
	v_fmac_f32_e32 v11, v8, v11
	s_waitcnt vmcnt(11)
	v_mfma_f32_32x32x16_bf16 v[18:33], v[110:113], v[158:161], v[18:33]
	v_rcp_f32_e32 v3, v3
	v_rcp_f32_e32 v2, v6
	v_rcp_f32_e32 v7, v10
	v_rcp_f32_e32 v6, v11
	s_waitcnt vmcnt(10)
	v_mfma_f32_32x32x16_bf16 v[18:33], v[106:109], v[154:157], v[18:33]
	v_exp_f32_e32 v183, v5
	v_exp_f32_e32 v186, v9
	s_waitcnt vmcnt(9)
	v_mfma_f32_32x32x16_bf16 v[18:33], v[102:105], v[142:145], v[18:33]
	v_fma_f32 v4, v178, s12, v184
	v_fma_f32 v5, v179, s12, v184
	v_exp_f32_e32 v178, v13
	v_pk_mul_f32 v[206:207], v[4:5], v[2:3]
	v_pk_fma_f32 v[2:3], v[180:181], s[12:13], v[184:185] op_sel_hi:[1,0,0]
	v_exp_f32_e32 v179, v17
	v_pk_mul_f32 v[208:209], v[2:3], v[6:7]
	s_waitcnt vmcnt(8)
	v_mfma_f32_32x32x16_bf16 v[18:33], v[98:101], v[130:133], v[18:33]
	v_mfma_f32_32x32x16_bf16 v[18:33], v[94:97], v[134:137], v[18:33]
	v_add_f32_e32 v180, 1.0, v183
	v_exp_f32_e32 v181, v207
	v_add_f32_e32 v183, 1.0, v186
	v_exp_f32_e32 v184, v206
	v_exp_f32_e32 v185, v209
	v_exp_f32_e32 v186, v208
	v_add_f32_e32 v178, 1.0, v178
	v_add_f32_e32 v179, 1.0, v179
	v_mfma_f32_32x32x16_bf16 v[18:33], v[90:93], v[138:141], v[18:33]
	v_fmac_f32_e32 v180, v180, v181
	v_fmac_f32_e32 v183, v183, v184
	v_fmac_f32_e32 v178, v178, v185
	v_fmac_f32_e32 v179, v179, v186
	v_mfma_f32_32x32x16_bf16 v[18:33], v[86:89], v[146:149], v[18:33]
	v_rcp_f32_e32 v180, v180
	v_rcp_f32_e32 v183, v183
	v_rcp_f32_e32 v178, v178
	v_rcp_f32_e32 v179, v179
	v_mfma_f32_32x32x16_bf16 v[18:33], v[82:85], v[150:153], v[18:33]
	v_fma_f32 v180, -v181, v180, v180
	v_fma_f32 v181, -v184, v183, v183
	v_fma_f32 v183, -v185, v178, v178
	v_fma_f32 v179, -v186, v179, v179
	v_cvt_pk_bf16_f32 v178, v180, v181
	v_cvt_pk_bf16_f32 v179, v183, v179
	ds_write_b64 v211, v[178:179] offset:8200
	s_waitcnt lgkmcnt(0)
	s_barrier
	v_mov_b32_e32 v178, 0x7a40
	v_lshl_add_u32 v232, v182, 2, v178
	s_mov_b32 s1, -1
	s_branch .LBB1_14

.Llight_path:
	s_waitcnt vmcnt(16)
	v_mul_u32_u24_e32 v236, 36, v228
	v_add_u32_e32 v236, v236, v230
	v_add_u32_e32 v237, s7, v229
	v_mul_u32_u24_e32 v238, 0x104, v228
	v_add_u32_e32 v238, v238, v237
	v_add_u32_e32 v238, 0xb440, v238
	ds_read_b128 v[2:5], v237 offset:36928
	ds_read_b128 v[6:9], v237 offset:36944
	ds_read_b128 v[10:13], v237 offset:36960
	ds_read_b128 v[14:17], v237 offset:36976
	ds_read_b128 v[18:21], v237 offset:37056
	ds_read_b128 v[22:25], v237 offset:37072
	ds_read_b128 v[26:29], v237 offset:37088
	ds_read_b128 v[30:33], v237 offset:37104
	ds_read_b128 v[162:165], v236 offset:16384
	ds_read_b128 v[166:169], v236 offset:16416
	ds_read_b128 v[170:173], v236 offset:16448
	ds_read_b128 v[174:177], v236 offset:16480
	s_waitcnt lgkmcnt(0)
	v_mfma_f32_32x32x16_bf16 v[2:17], v[94:97], v[162:165], v[2:17]
	v_mfma_f32_32x32x16_bf16 v[2:17], v[90:93], v[166:169], v[2:17]
	v_mfma_f32_32x32x16_bf16 v[2:17], v[86:89], v[170:173], v[2:17]
	v_mfma_f32_32x32x16_bf16 v[2:17], v[82:85], v[174:177], v[2:17]
	v_mfma_f32_32x32x16_bf16 v[18:33], v[46:49], v[162:165], v[18:33]
	ds_read_b128 v[130:133], v237 offset:36928
	ds_read_b128 v[134:137], v237 offset:36944
	ds_read_b128 v[138:141], v237 offset:36960
	v_mfma_f32_32x32x16_bf16 v[18:33], v[42:45], v[166:169], v[18:33]
	ds_read_b128 v[142:145], v237 offset:36976
	ds_read_b128 v[146:149], v237 offset:37056
	ds_read_b128 v[150:153], v237 offset:37072
	v_mfma_f32_32x32x16_bf16 v[18:33], v[38:41], v[170:173], v[18:33]
	ds_read_b128 v[154:157], v237 offset:37088
	ds_read_b128 v[158:161], v237 offset:37104
	ds_read_b128 v[178:181], v236 offset:20992
	v_mfma_f32_32x32x16_bf16 v[18:33], v[34:37], v[174:177], v[18:33]
	ds_read_b128 v[182:185], v236 offset:21024
	ds_read_b128 v[186:189], v236 offset:21056
	ds_read_b128 v[190:193], v236 offset:21088
	s_waitcnt lgkmcnt(0)
	v_mfma_f32_32x32x16_bf16 v[130:145], v[94:97], v[178:181], v[130:145]
	v_mfma_f32_32x32x16_bf16 v[130:145], v[90:93], v[182:185], v[130:145]
	v_mfma_f32_32x32x16_bf16 v[130:145], v[86:89], v[186:189], v[130:145]
	v_mfma_f32_32x32x16_bf16 v[130:145], v[82:85], v[190:193], v[130:145]
	s_nop 7
	ds_write_b128 v238, v[2:5] offset:0
	ds_write_b128 v238, v[6:9] offset:16
	ds_write_b128 v238, v[10:13] offset:32
	ds_write_b128 v238, v[14:17] offset:48
	ds_write_b128 v238, v[18:21] offset:128
	ds_write_b128 v238, v[22:25] offset:144
	ds_write_b128 v238, v[26:29] offset:160
	ds_write_b128 v238, v[30:33] offset:176
	v_mfma_f32_32x32x16_bf16 v[146:161], v[46:49], v[178:181], v[146:161]
	ds_read_b128 v[2:5], v237 offset:36928
	ds_read_b128 v[6:9], v237 offset:36944
	ds_read_b128 v[10:13], v237 offset:36960
	v_mfma_f32_32x32x16_bf16 v[146:161], v[42:45], v[182:185], v[146:161]
	ds_read_b128 v[14:17], v237 offset:36976
	ds_read_b128 v[18:21], v237 offset:37056
	ds_read_b128 v[22:25], v237 offset:37072
	v_mfma_f32_32x32x16_bf16 v[146:161], v[38:41], v[186:189], v[146:161]
	ds_read_b128 v[26:29], v237 offset:37088
	ds_read_b128 v[30:33], v237 offset:37104
	ds_read_b128 v[162:165], v236 offset:25600
	v_mfma_f32_32x32x16_bf16 v[146:161], v[34:37], v[190:193], v[146:161]
	ds_read_b128 v[166:169], v236 offset:25632
	ds_read_b128 v[170:173], v236 offset:25664
	ds_read_b128 v[174:177], v236 offset:25696
	s_waitcnt lgkmcnt(0)
	v_mfma_f32_32x32x16_bf16 v[2:17], v[94:97], v[162:165], v[2:17]
	v_mfma_f32_32x32x16_bf16 v[2:17], v[90:93], v[166:169], v[2:17]
	v_mfma_f32_32x32x16_bf16 v[2:17], v[86:89], v[170:173], v[2:17]
	v_mfma_f32_32x32x16_bf16 v[2:17], v[82:85], v[174:177], v[2:17]
	s_nop 7
	v_add_u32_e32 v239, 0x8200, v238
	ds_write_b128 v239, v[130:133] offset:0
	ds_write_b128 v239, v[134:137] offset:16
	ds_write_b128 v239, v[138:141] offset:32
	ds_write_b128 v239, v[142:145] offset:48
	ds_write_b128 v239, v[146:149] offset:128
	ds_write_b128 v239, v[150:153] offset:144
	ds_write_b128 v239, v[154:157] offset:160
	ds_write_b128 v239, v[158:161] offset:176
	v_mfma_f32_32x32x16_bf16 v[18:33], v[46:49], v[162:165], v[18:33]
	ds_read_b128 v[130:133], v237 offset:36928
	ds_read_b128 v[134:137], v237 offset:36944
	ds_read_b128 v[138:141], v237 offset:36960
	v_mfma_f32_32x32x16_bf16 v[18:33], v[42:45], v[166:169], v[18:33]
	ds_read_b128 v[142:145], v237 offset:36976
	ds_read_b128 v[146:149], v237 offset:37056
	ds_read_b128 v[150:153], v237 offset:37072
	v_mfma_f32_32x32x16_bf16 v[18:33], v[38:41], v[170:173], v[18:33]
	ds_read_b128 v[154:157], v237 offset:37088
	ds_read_b128 v[158:161], v237 offset:37104
	ds_read_b128 v[178:181], v236 offset:30208
	v_mfma_f32_32x32x16_bf16 v[18:33], v[34:37], v[174:177], v[18:33]
	ds_read_b128 v[182:185], v236 offset:30240
	ds_read_b128 v[186:189], v236 offset:30272
	ds_read_b128 v[190:193], v236 offset:30304
	s_waitcnt lgkmcnt(0)
	v_mfma_f32_32x32x16_bf16 v[130:145], v[94:97], v[178:181], v[130:145]
	v_mfma_f32_32x32x16_bf16 v[130:145], v[90:93], v[182:185], v[130:145]
	v_mfma_f32_32x32x16_bf16 v[130:145], v[86:89], v[186:189], v[130:145]
	v_mfma_f32_32x32x16_bf16 v[130:145], v[82:85], v[190:193], v[130:145]
	s_nop 7
	v_add_u32_e32 v239, 0x10400, v238
	ds_write_b128 v239, v[2:5] offset:0
	ds_write_b128 v239, v[6:9] offset:16
	ds_write_b128 v239, v[10:13] offset:32
	ds_write_b128 v239, v[14:17] offset:48
	ds_write_b128 v239, v[18:21] offset:128
	ds_write_b128 v239, v[22:25] offset:144
	ds_write_b128 v239, v[26:29] offset:160
	ds_write_b128 v239, v[30:33] offset:176
	v_mfma_f32_32x32x16_bf16 v[146:161], v[46:49], v[178:181], v[146:161]
	v_mfma_f32_32x32x16_bf16 v[146:161], v[42:45], v[182:185], v[146:161]
	v_mfma_f32_32x32x16_bf16 v[146:161], v[38:41], v[186:189], v[146:161]
	v_mfma_f32_32x32x16_bf16 v[146:161], v[34:37], v[190:193], v[146:161]
	s_nop 7
	s_nop 7
	v_cmp_gt_u32_e32 vcc, 16, v228
	s_and_saveexec_b64 s[20:21], vcc
	v_add_u32_e32 v239, 0x18600, v238
	ds_write_b128 v239, v[130:133] offset:0
	ds_write_b128 v239, v[134:137] offset:16
	ds_write_b128 v239, v[138:141] offset:32
	ds_write_b128 v239, v[142:145] offset:48
	ds_write_b128 v239, v[146:149] offset:128
	ds_write_b128 v239, v[150:153] offset:144
	ds_write_b128 v239, v[154:157] offset:160
	ds_write_b128 v239, v[158:161] offset:176
	s_or_b64 exec, exec, s[20:21]
	s_waitcnt vmcnt(0) lgkmcnt(0)
	s_nop 7
	s_nop 7
	s_waitcnt vmcnt(0)
	v_add_u32_e32 v231, s7, v229
	v_add_u32_e32 v231, 0xb440, v231
	v_add_u32_e32 v211, s6, v210
	s_mov_b32 s12, 0x4038aa3b
	v_mov_b32_e32 v235, 0xc038aa3b
	s_nop 0
	s_load_dwordx8 s[4:11], s[0:1], 0x10
	s_waitcnt lgkmcnt(0)
	v_add_u32_e32 v232, 0x24e80, v228
	ds_read_b32 v244, v232
	ds_read_b32 v245, v232 offset:128
	v_mov_b32_e32 v194, 0
	v_mov_b32_e32 v195, 0
	v_mov_b32_e32 v196, 0
	v_mov_b32_e32 v197, 0
	v_mov_b32_e32 v198, 0
	v_mov_b32_e32 v199, 0
	v_mov_b32_e32 v200, 0
	v_mov_b32_e32 v201, 0
	v_mov_b32_e32 v202, 0
	v_mov_b32_e32 v203, 0
	v_mov_b32_e32 v204, 0
	v_mov_b32_e32 v205, 0
	v_mov_b32_e32 v206, 0
	v_mov_b32_e32 v207, 0
	v_mov_b32_e32 v208, 0
	v_mov_b32_e32 v209, 0
	v_add_u32_e32 v232, 0x100, v232
	s_waitcnt lgkmcnt(0)
	v_add_u32_e32 v233, v231, v244
	v_add_u32_e32 v234, v231, v245
	ds_read_b128 v[2:5], v233 offset:0
	ds_read_b128 v[6:9], v233 offset:16
	ds_read_b128 v[10:13], v233 offset:32
	ds_read_b128 v[14:17], v233 offset:48
	ds_read_b128 v[18:21], v233 offset:128
	ds_read_b128 v[22:25], v233 offset:144
	ds_read_b128 v[26:29], v233 offset:160
	ds_read_b128 v[30:33], v233 offset:176
	ds_read_b128 v[34:37], v234 offset:0
	ds_read_b128 v[38:41], v234 offset:16
	ds_read_b128 v[42:45], v234 offset:32
	ds_read_b128 v[46:49], v234 offset:48
	s_movk_i32 s16, 18
	s_waitcnt lgkmcnt(0)
	ds_read_b128 v[82:85], v234 offset:128
	ds_read_b128 v[86:89], v234 offset:144
	ds_read_b128 v[90:93], v234 offset:160
	ds_read_b128 v[94:97], v234 offset:176
	ds_read_b32 v244, v232 offset:0
	v_exp_f32_e32 v212, v4
	v_exp_f32_e32 v213, v8
	v_exp_f32_e32 v214, v12
	v_exp_f32_e32 v215, v16
	v_exp_f32_e32 v216, v2
	v_add_f32_e32 v236, 1.0, v212
	v_exp_f32_e32 v217, v6
	v_add_f32_e32 v237, 1.0, v213
	v_exp_f32_e32 v218, v10
	v_add_f32_e32 v238, 1.0, v214
	v_exp_f32_e32 v219, v14
	v_add_f32_e32 v239, 1.0, v215
	v_fma_f32 v240, v212, s12, v235
	v_fma_f32 v241, v213, s12, v235
	v_fma_f32 v242, v214, s12, v235
	v_fma_f32 v243, v215, s12, v235
	v_fmac_f32_e32 v236, v216, v236
	v_fmac_f32_e32 v237, v217, v237
	v_fmac_f32_e32 v238, v218, v238
	v_fmac_f32_e32 v239, v219, v239
	v_rcp_f32_e32 v216, v236
	v_rcp_f32_e32 v217, v237
	v_rcp_f32_e32 v218, v238
	v_rcp_f32_e32 v219, v239
	v_exp_f32_e32 v224, v5
	v_mul_f32_e32 v194, v240, v216
	v_exp_f32_e32 v225, v9
	v_mul_f32_e32 v195, v241, v217
	v_exp_f32_e32 v226, v13
	v_mul_f32_e32 v196, v242, v218
	v_exp_f32_e32 v227, v17
	v_mul_f32_e32 v197, v243, v219
	v_exp_f32_e32 v212, v194
	v_add_f32_e32 v224, 1.0, v224
	v_exp_f32_e32 v213, v195
	v_add_f32_e32 v225, 1.0, v225
	v_exp_f32_e32 v214, v196
	v_add_f32_e32 v226, 1.0, v226
	v_exp_f32_e32 v215, v197
	v_add_f32_e32 v227, 1.0, v227
	v_fmac_f32_e32 v224, v224, v212
	v_fmac_f32_e32 v225, v225, v213
	v_fmac_f32_e32 v226, v226, v214
	v_fmac_f32_e32 v227, v227, v215
	v_rcp_f32_e32 v224, v224
	v_rcp_f32_e32 v225, v225
	v_rcp_f32_e32 v226, v226
	v_rcp_f32_e32 v227, v227
	v_fma_f32 v224, -v212, v224, v224
	v_fma_f32 v225, -v213, v225, v225
	v_fma_f32 v226, -v214, v226, v226
	v_fma_f32 v227, -v215, v227, v227
	v_cvt_pk_bf16_f32 v224, v224, v225
	v_cvt_pk_bf16_f32 v225, v226, v227
	ds_write_b64 v211, v[224:225] offset:0
	s_waitcnt lgkmcnt(1)
	v_add_u32_e32 v233, v231, v244
	ds_read_b128 v[2:5], v233 offset:0
	ds_read_b128 v[6:9], v233 offset:16
	ds_read_b128 v[10:13], v233 offset:32
	ds_read_b128 v[14:17], v233 offset:48
	v_exp_f32_e32 v212, v20
	v_exp_f32_e32 v213, v24
	v_exp_f32_e32 v214, v28
	v_exp_f32_e32 v215, v32
	v_exp_f32_e32 v216, v18
	v_add_f32_e32 v236, 1.0, v212
	v_exp_f32_e32 v217, v22
	v_add_f32_e32 v237, 1.0, v213
	v_exp_f32_e32 v218, v26
	v_add_f32_e32 v238, 1.0, v214
	v_exp_f32_e32 v219, v30
	v_add_f32_e32 v239, 1.0, v215
	v_fma_f32 v240, v212, s12, v235
	v_fma_f32 v241, v213, s12, v235
	v_fma_f32 v242, v214, s12, v235
	v_fma_f32 v243, v215, s12, v235
	v_fmac_f32_e32 v236, v216, v236
	v_fmac_f32_e32 v237, v217, v237
	v_fmac_f32_e32 v238, v218, v238
	v_fmac_f32_e32 v239, v219, v239
	v_rcp_f32_e32 v216, v236
	v_rcp_f32_e32 v217, v237
	v_rcp_f32_e32 v218, v238
	v_rcp_f32_e32 v219, v239
	v_exp_f32_e32 v224, v21
	v_mul_f32_e32 v198, v240, v216
	v_exp_f32_e32 v225, v25
	v_mul_f32_e32 v199, v241, v217
	v_exp_f32_e32 v226, v29
	v_mul_f32_e32 v200, v242, v218
	v_exp_f32_e32 v227, v33
	v_mul_f32_e32 v201, v243, v219
	v_exp_f32_e32 v212, v198
	v_add_f32_e32 v224, 1.0, v224
	v_exp_f32_e32 v213, v199
	v_add_f32_e32 v225, 1.0, v225
	v_exp_f32_e32 v214, v200
	v_add_f32_e32 v226, 1.0, v226
	v_exp_f32_e32 v215, v201
	v_add_f32_e32 v227, 1.0, v227
	v_fmac_f32_e32 v224, v224, v212
	v_fmac_f32_e32 v225, v225, v213
	v_fmac_f32_e32 v226, v226, v214
	v_fmac_f32_e32 v227, v227, v215
	v_rcp_f32_e32 v224, v224
	v_rcp_f32_e32 v225, v225
	v_rcp_f32_e32 v226, v226
	v_rcp_f32_e32 v227, v227
	v_fma_f32 v224, -v212, v224, v224
	v_fma_f32 v225, -v213, v225, v225
	v_fma_f32 v226, -v214, v226, v226
	v_fma_f32 v227, -v215, v227, v227
	v_cvt_pk_bf16_f32 v224, v224, v225
	v_cvt_pk_bf16_f32 v225, v226, v227
	ds_write_b64 v211, v[224:225] offset:8
	s_waitcnt lgkmcnt(0)
	s_barrier
	ds_read_b128 v[130:133], v210 offset:0
	ds_read_b128 v[134:137], v210 offset:1024
	ds_read_b128 v[18:21], v233 offset:128
	ds_read_b128 v[22:25], v233 offset:144
	ds_read_b128 v[26:29], v233 offset:160
	ds_read_b128 v[30:33], v233 offset:176
	ds_read_b32 v245, v232 offset:128
	v_exp_f32_e32 v212, v36
	v_exp_f32_e32 v213, v40
	v_exp_f32_e32 v214, v44
	v_exp_f32_e32 v215, v48
	ds_read_b128 v[138:141], v210 offset:2048
	ds_read_b128 v[142:145], v210 offset:3072
	v_exp_f32_e32 v216, v34
	v_add_f32_e32 v236, 1.0, v212
	v_exp_f32_e32 v217, v38
	v_add_f32_e32 v237, 1.0, v213
	v_exp_f32_e32 v218, v42
	v_add_f32_e32 v238, 1.0, v214
	v_exp_f32_e32 v219, v46
	v_add_f32_e32 v239, 1.0, v215
	v_fma_f32 v240, v212, s12, v235
	v_fma_f32 v241, v213, s12, v235
	v_fma_f32 v242, v214, s12, v235
	v_fma_f32 v243, v215, s12, v235
	ds_read_b128 v[146:149], v210 offset:4096
	ds_read_b128 v[150:153], v210 offset:5120
	v_fmac_f32_e32 v236, v216, v236
	v_fmac_f32_e32 v237, v217, v237
	v_fmac_f32_e32 v238, v218, v238
	v_fmac_f32_e32 v239, v219, v239
	ds_read_b128 v[154:157], v210 offset:6144
	ds_read_b128 v[158:161], v210 offset:7168
	v_rcp_f32_e32 v216, v236
	v_rcp_f32_e32 v217, v237
	v_rcp_f32_e32 v218, v238
	v_rcp_f32_e32 v219, v239
	v_exp_f32_e32 v224, v37
	v_mul_f32_e32 v202, v240, v216
	v_exp_f32_e32 v225, v41
	v_mul_f32_e32 v203, v241, v217
	v_exp_f32_e32 v226, v45
	v_mul_f32_e32 v204, v242, v218
	v_exp_f32_e32 v227, v49
	v_mul_f32_e32 v205, v243, v219
	v_exp_f32_e32 v212, v202
	v_add_f32_e32 v224, 1.0, v224
	v_exp_f32_e32 v213, v203
	v_add_f32_e32 v225, 1.0, v225
	v_exp_f32_e32 v214, v204
	v_add_f32_e32 v226, 1.0, v226
	v_exp_f32_e32 v215, v205
	v_add_f32_e32 v227, 1.0, v227
	v_fmac_f32_e32 v224, v224, v212
	v_fmac_f32_e32 v225, v225, v213
	v_fmac_f32_e32 v226, v226, v214
	v_fmac_f32_e32 v227, v227, v215
	v_rcp_f32_e32 v224, v224
	v_rcp_f32_e32 v225, v225
	v_rcp_f32_e32 v226, v226
	v_rcp_f32_e32 v227, v227
	v_fma_f32 v224, -v212, v224, v224
	v_fma_f32 v225, -v213, v225, v225
	v_fma_f32 v226, -v214, v226, v226
	v_fma_f32 v227, -v215, v227, v227
	v_cvt_pk_bf16_f32 v224, v224, v225
	v_cvt_pk_bf16_f32 v225, v226, v227
	ds_write_b64 v211, v[224:225] offset:8192
	s_waitcnt lgkmcnt(1)
	v_mfma_f32_32x32x16_bf16 v[2:17], v[126:129], v[130:133], v[2:17]
	v_add_u32_e32 v234, v231, v245
	ds_read_b128 v[34:37], v234 offset:0
	ds_read_b128 v[38:41], v234 offset:16
	ds_read_b128 v[42:45], v234 offset:32
	ds_read_b128 v[46:49], v234 offset:48
	v_add_u32_e32 v232, 0x100, v232
	v_exp_f32_e32 v212, v84
	v_exp_f32_e32 v213, v88
	v_exp_f32_e32 v214, v92
	v_exp_f32_e32 v215, v96
	v_mfma_f32_32x32x16_bf16 v[2:17], v[122:125], v[134:137], v[2:17]
	v_exp_f32_e32 v216, v82
	v_add_f32_e32 v236, 1.0, v212
	v_exp_f32_e32 v217, v86
	v_add_f32_e32 v237, 1.0, v213
	v_exp_f32_e32 v218, v90
	v_add_f32_e32 v238, 1.0, v214
	v_exp_f32_e32 v219, v94
	v_add_f32_e32 v239, 1.0, v215
	v_fma_f32 v240, v212, s12, v235
	v_fma_f32 v241, v213, s12, v235
	v_fma_f32 v242, v214, s12, v235
	v_fma_f32 v243, v215, s12, v235
	v_mfma_f32_32x32x16_bf16 v[2:17], v[118:121], v[138:141], v[2:17]
	v_fmac_f32_e32 v236, v216, v236
	v_fmac_f32_e32 v237, v217, v237
	v_fmac_f32_e32 v238, v218, v238
	v_fmac_f32_e32 v239, v219, v239
	v_mfma_f32_32x32x16_bf16 v[2:17], v[114:117], v[142:145], v[2:17]
	v_rcp_f32_e32 v216, v236
	v_rcp_f32_e32 v217, v237
	v_rcp_f32_e32 v218, v238
	v_rcp_f32_e32 v219, v239
	v_mfma_f32_32x32x16_bf16 v[2:17], v[110:113], v[146:149], v[2:17]
	v_exp_f32_e32 v224, v85
	v_mul_f32_e32 v206, v240, v216
	v_exp_f32_e32 v225, v89
	v_mul_f32_e32 v207, v241, v217
	v_exp_f32_e32 v226, v93
	v_mul_f32_e32 v208, v242, v218
	v_exp_f32_e32 v227, v97
	v_mul_f32_e32 v209, v243, v219
	v_mfma_f32_32x32x16_bf16 v[2:17], v[106:109], v[150:153], v[2:17]
	v_mfma_f32_32x32x16_bf16 v[2:17], v[102:105], v[154:157], v[2:17]
	v_exp_f32_e32 v212, v206
	v_add_f32_e32 v224, 1.0, v224
	v_exp_f32_e32 v213, v207
	v_add_f32_e32 v225, 1.0, v225
	v_exp_f32_e32 v214, v208
	v_add_f32_e32 v226, 1.0, v226
	v_exp_f32_e32 v215, v209
	v_add_f32_e32 v227, 1.0, v227
	v_fmac_f32_e32 v224, v224, v212
	v_fmac_f32_e32 v225, v225, v213
	v_fmac_f32_e32 v226, v226, v214
	v_fmac_f32_e32 v227, v227, v215
	v_mfma_f32_32x32x16_bf16 v[2:17], v[98:101], v[158:161], v[2:17]
	v_rcp_f32_e32 v224, v224
	v_rcp_f32_e32 v225, v225
	v_rcp_f32_e32 v226, v226
	v_rcp_f32_e32 v227, v227
	v_fma_f32 v224, -v212, v224, v224
	v_fma_f32 v225, -v213, v225, v225
	v_fma_f32 v226, -v214, v226, v226
	v_fma_f32 v227, -v215, v227, v227
	v_cvt_pk_bf16_f32 v224, v224, v225
	v_cvt_pk_bf16_f32 v225, v226, v227
	ds_write_b64 v211, v[224:225] offset:8200
	s_waitcnt lgkmcnt(0)
	s_barrier
.Llight_loop:
	v_mfma_f32_32x32x16_bf16 v[18:33], v[78:81], v[130:133], v[18:33]
	ds_read_b128 v[162:165], v210 offset:8192
	ds_read_b128 v[166:169], v210 offset:9216
	ds_read_b128 v[82:85], v234 offset:128
	ds_read_b128 v[86:89], v234 offset:144
	ds_read_b128 v[90:93], v234 offset:160
	ds_read_b128 v[94:97], v234 offset:176
	ds_read_b32 v244, v232 offset:0
	v_exp_f32_e32 v212, v4
	v_exp_f32_e32 v213, v8
	v_exp_f32_e32 v214, v12
	v_exp_f32_e32 v215, v16
	v_mfma_f32_32x32x16_bf16 v[18:33], v[74:77], v[134:137], v[18:33]
	ds_read_b128 v[170:173], v210 offset:10240
	ds_read_b128 v[174:177], v210 offset:11264
	v_exp_f32_e32 v216, v2
	v_add_f32_e32 v236, 1.0, v212
	v_exp_f32_e32 v217, v6
	v_add_f32_e32 v237, 1.0, v213
	v_exp_f32_e32 v218, v10
	v_add_f32_e32 v238, 1.0, v214
	v_exp_f32_e32 v219, v14
	v_add_f32_e32 v239, 1.0, v215
	v_fma_f32 v240, v212, s12, v235
	v_fma_f32 v241, v213, s12, v235
	v_fma_f32 v242, v214, s12, v235
	v_fma_f32 v243, v215, s12, v235
	v_mfma_f32_32x32x16_bf16 v[18:33], v[70:73], v[138:141], v[18:33]
	ds_read_b128 v[178:181], v210 offset:12288
	ds_read_b128 v[182:185], v210 offset:13312
	v_exp_f32_e32 v220, v3
	v_fmac_f32_e32 v236, v216, v236
	v_exp_f32_e32 v221, v7
	v_fmac_f32_e32 v237, v217, v237
	v_exp_f32_e32 v222, v11
	v_fmac_f32_e32 v238, v218, v238
	v_exp_f32_e32 v223, v15
	v_fmac_f32_e32 v239, v219, v239
	v_mfma_f32_32x32x16_bf16 v[18:33], v[66:69], v[142:145], v[18:33]
	ds_read_b128 v[186:189], v210 offset:14336
	ds_read_b128 v[190:193], v210 offset:15360
	v_rcp_f32_e32 v216, v236
	v_add_f32_e32 v220, 1.0, v220
	v_rcp_f32_e32 v217, v237
	v_add_f32_e32 v221, 1.0, v221
	v_rcp_f32_e32 v218, v238
	v_add_f32_e32 v222, 1.0, v222
	v_rcp_f32_e32 v219, v239
	v_add_f32_e32 v223, 1.0, v223
	v_mfma_f32_32x32x16_bf16 v[18:33], v[62:65], v[146:149], v[18:33]
	v_rcp_f32_e32 v220, v220
	v_mul_f32_e32 v240, v240, v216
	v_rcp_f32_e32 v221, v221
	v_mul_f32_e32 v241, v241, v217
	v_rcp_f32_e32 v222, v222
	v_mul_f32_e32 v242, v242, v218
	v_rcp_f32_e32 v223, v223
	v_mul_f32_e32 v243, v243, v219
	v_mfma_f32_32x32x16_bf16 v[18:33], v[58:61], v[150:153], v[18:33]
	v_exp_f32_e32 v224, v5
	v_fma_f32 v194, v220, v194, v240
	v_exp_f32_e32 v225, v9
	v_fma_f32 v195, v221, v195, v241
	v_exp_f32_e32 v226, v13
	v_fma_f32 v196, v222, v196, v242
	v_exp_f32_e32 v227, v17
	v_fma_f32 v197, v223, v197, v243
	v_mfma_f32_32x32x16_bf16 v[18:33], v[54:57], v[154:157], v[18:33]
	v_exp_f32_e32 v212, v194
	v_add_f32_e32 v224, 1.0, v224
	v_exp_f32_e32 v213, v195
	v_add_f32_e32 v225, 1.0, v225
	v_exp_f32_e32 v214, v196
	v_add_f32_e32 v226, 1.0, v226
	v_exp_f32_e32 v215, v197
	v_add_f32_e32 v227, 1.0, v227
	v_fmac_f32_e32 v224, v224, v212
	v_fmac_f32_e32 v225, v225, v213
	v_fmac_f32_e32 v226, v226, v214
	v_fmac_f32_e32 v227, v227, v215
	v_mfma_f32_32x32x16_bf16 v[18:33], v[50:53], v[158:161], v[18:33]
	v_rcp_f32_e32 v224, v224
	v_rcp_f32_e32 v225, v225
	v_rcp_f32_e32 v226, v226
	v_rcp_f32_e32 v227, v227
	v_fma_f32 v224, -v212, v224, v224
	v_fma_f32 v225, -v213, v225, v225
	v_fma_f32 v226, -v214, v226, v226
	v_fma_f32 v227, -v215, v227, v227
	v_cvt_pk_bf16_f32 v224, v224, v225
	v_cvt_pk_bf16_f32 v225, v226, v227
	ds_write_b64 v211, v[224:225] offset:0
	s_waitcnt lgkmcnt(1)
	v_mfma_f32_32x32x16_bf16 v[34:49], v[126:129], v[162:165], v[34:49]
	v_add_u32_e32 v233, v231, v244
	ds_read_b128 v[2:5], v233 offset:0
	ds_read_b128 v[6:9], v233 offset:16
	ds_read_b128 v[10:13], v233 offset:32
	ds_read_b128 v[14:17], v233 offset:48
	v_exp_f32_e32 v212, v20
	v_exp_f32_e32 v213, v24
	v_exp_f32_e32 v214, v28
	v_exp_f32_e32 v215, v32
	v_mfma_f32_32x32x16_bf16 v[34:49], v[122:125], v[166:169], v[34:49]
	v_exp_f32_e32 v216, v18
	v_add_f32_e32 v236, 1.0, v212
	v_exp_f32_e32 v217, v22
	v_add_f32_e32 v237, 1.0, v213
	v_exp_f32_e32 v218, v26
	v_add_f32_e32 v238, 1.0, v214
	v_exp_f32_e32 v219, v30
	v_add_f32_e32 v239, 1.0, v215
	v_fma_f32 v240, v212, s12, v235
	v_fma_f32 v241, v213, s12, v235
	v_fma_f32 v242, v214, s12, v235
	v_fma_f32 v243, v215, s12, v235
	v_mfma_f32_32x32x16_bf16 v[34:49], v[118:121], v[170:173], v[34:49]
	v_exp_f32_e32 v220, v19
	v_fmac_f32_e32 v236, v216, v236
	v_exp_f32_e32 v221, v23
	v_fmac_f32_e32 v237, v217, v237
	v_exp_f32_e32 v222, v27
	v_fmac_f32_e32 v238, v218, v238
	v_exp_f32_e32 v223, v31
	v_fmac_f32_e32 v239, v219, v239
	v_mfma_f32_32x32x16_bf16 v[34:49], v[114:117], v[174:177], v[34:49]
	v_rcp_f32_e32 v216, v236
	v_add_f32_e32 v220, 1.0, v220
	v_rcp_f32_e32 v217, v237
	v_add_f32_e32 v221, 1.0, v221
	v_rcp_f32_e32 v218, v238
	v_add_f32_e32 v222, 1.0, v222
	v_rcp_f32_e32 v219, v239
	v_add_f32_e32 v223, 1.0, v223
	v_mfma_f32_32x32x16_bf16 v[34:49], v[110:113], v[178:181], v[34:49]
	v_rcp_f32_e32 v220, v220
	v_mul_f32_e32 v240, v240, v216
	v_rcp_f32_e32 v221, v221
	v_mul_f32_e32 v241, v241, v217
	v_rcp_f32_e32 v222, v222
	v_mul_f32_e32 v242, v242, v218
	v_rcp_f32_e32 v223, v223
	v_mul_f32_e32 v243, v243, v219
	v_mfma_f32_32x32x16_bf16 v[34:49], v[106:109], v[182:185], v[34:49]
	v_exp_f32_e32 v224, v21
	v_fma_f32 v198, v220, v198, v240
	v_exp_f32_e32 v225, v25
	v_fma_f32 v199, v221, v199, v241
	v_exp_f32_e32 v226, v29
	v_fma_f32 v200, v222, v200, v242
	v_exp_f32_e32 v227, v33
	v_fma_f32 v201, v223, v201, v243
	v_mfma_f32_32x32x16_bf16 v[34:49], v[102:105], v[186:189], v[34:49]
	v_exp_f32_e32 v212, v198
	v_add_f32_e32 v224, 1.0, v224
	v_exp_f32_e32 v213, v199
	v_add_f32_e32 v225, 1.0, v225
	v_exp_f32_e32 v214, v200
	v_add_f32_e32 v226, 1.0, v226
	v_exp_f32_e32 v215, v201
	v_add_f32_e32 v227, 1.0, v227
	v_fmac_f32_e32 v224, v224, v212
	v_fmac_f32_e32 v225, v225, v213
	v_fmac_f32_e32 v226, v226, v214
	v_fmac_f32_e32 v227, v227, v215
	v_mfma_f32_32x32x16_bf16 v[34:49], v[98:101], v[190:193], v[34:49]
	v_rcp_f32_e32 v224, v224
	v_rcp_f32_e32 v225, v225
	v_rcp_f32_e32 v226, v226
	v_rcp_f32_e32 v227, v227
	v_fma_f32 v224, -v212, v224, v224
	v_fma_f32 v225, -v213, v225, v225
	v_fma_f32 v226, -v214, v226, v226
	v_fma_f32 v227, -v215, v227, v227
	v_cvt_pk_bf16_f32 v224, v224, v225
	v_cvt_pk_bf16_f32 v225, v226, v227
	ds_write_b64 v211, v[224:225] offset:8
	s_waitcnt lgkmcnt(0)
	s_barrier
	v_mfma_f32_32x32x16_bf16 v[82:97], v[78:81], v[162:165], v[82:97]
	ds_read_b128 v[130:133], v210 offset:0
	ds_read_b128 v[134:137], v210 offset:1024
	ds_read_b128 v[18:21], v233 offset:128
	ds_read_b128 v[22:25], v233 offset:144
	ds_read_b128 v[26:29], v233 offset:160
	ds_read_b128 v[30:33], v233 offset:176
	ds_read_b32 v245, v232 offset:128
	v_exp_f32_e32 v212, v36
	v_exp_f32_e32 v213, v40
	v_exp_f32_e32 v214, v44
	v_exp_f32_e32 v215, v48
	v_mfma_f32_32x32x16_bf16 v[82:97], v[74:77], v[166:169], v[82:97]
	ds_read_b128 v[138:141], v210 offset:2048
	ds_read_b128 v[142:145], v210 offset:3072
	v_exp_f32_e32 v216, v34
	v_add_f32_e32 v236, 1.0, v212
	v_exp_f32_e32 v217, v38
	v_add_f32_e32 v237, 1.0, v213
	v_exp_f32_e32 v218, v42
	v_add_f32_e32 v238, 1.0, v214
	v_exp_f32_e32 v219, v46
	v_add_f32_e32 v239, 1.0, v215
	v_fma_f32 v240, v212, s12, v235
	v_fma_f32 v241, v213, s12, v235
	v_fma_f32 v242, v214, s12, v235
	v_fma_f32 v243, v215, s12, v235
	v_mfma_f32_32x32x16_bf16 v[82:97], v[70:73], v[170:173], v[82:97]
	ds_read_b128 v[146:149], v210 offset:4096
	ds_read_b128 v[150:153], v210 offset:5120
	v_exp_f32_e32 v220, v35
	v_fmac_f32_e32 v236, v216, v236
	v_exp_f32_e32 v221, v39
	v_fmac_f32_e32 v237, v217, v237
	v_exp_f32_e32 v222, v43
	v_fmac_f32_e32 v238, v218, v238
	v_exp_f32_e32 v223, v47
	v_fmac_f32_e32 v239, v219, v239
	v_mfma_f32_32x32x16_bf16 v[82:97], v[66:69], v[174:177], v[82:97]
	ds_read_b128 v[154:157], v210 offset:6144
	ds_read_b128 v[158:161], v210 offset:7168
	v_rcp_f32_e32 v216, v236
	v_add_f32_e32 v220, 1.0, v220
	v_rcp_f32_e32 v217, v237
	v_add_f32_e32 v221, 1.0, v221
	v_rcp_f32_e32 v218, v238
	v_add_f32_e32 v222, 1.0, v222
	v_rcp_f32_e32 v219, v239
	v_add_f32_e32 v223, 1.0, v223
	v_mfma_f32_32x32x16_bf16 v[82:97], v[62:65], v[178:181], v[82:97]
	v_rcp_f32_e32 v220, v220
	v_mul_f32_e32 v240, v240, v216
	v_rcp_f32_e32 v221, v221
	v_mul_f32_e32 v241, v241, v217
	v_rcp_f32_e32 v222, v222
	v_mul_f32_e32 v242, v242, v218
	v_rcp_f32_e32 v223, v223
	v_mul_f32_e32 v243, v243, v219
	v_mfma_f32_32x32x16_bf16 v[82:97], v[58:61], v[182:185], v[82:97]
	v_exp_f32_e32 v224, v37
	v_fma_f32 v202, v220, v202, v240
	v_exp_f32_e32 v225, v41
	v_fma_f32 v203, v221, v203, v241
	v_exp_f32_e32 v226, v45
	v_fma_f32 v204, v222, v204, v242
	v_exp_f32_e32 v227, v49
	v_fma_f32 v205, v223, v205, v243
	v_mfma_f32_32x32x16_bf16 v[82:97], v[54:57], v[186:189], v[82:97]
	v_exp_f32_e32 v212, v202
	v_add_f32_e32 v224, 1.0, v224
	v_exp_f32_e32 v213, v203
	v_add_f32_e32 v225, 1.0, v225
	v_exp_f32_e32 v214, v204
	v_add_f32_e32 v226, 1.0, v226
	v_exp_f32_e32 v215, v205
	v_add_f32_e32 v227, 1.0, v227
	v_fmac_f32_e32 v224, v224, v212
	v_fmac_f32_e32 v225, v225, v213
	v_fmac_f32_e32 v226, v226, v214
	v_fmac_f32_e32 v227, v227, v215
	v_mfma_f32_32x32x16_bf16 v[82:97], v[50:53], v[190:193], v[82:97]
	v_rcp_f32_e32 v224, v224
	v_rcp_f32_e32 v225, v225
	v_rcp_f32_e32 v226, v226
	v_rcp_f32_e32 v227, v227
	v_fma_f32 v224, -v212, v224, v224
	v_fma_f32 v225, -v213, v225, v225
	v_fma_f32 v226, -v214, v226, v226
	v_fma_f32 v227, -v215, v227, v227
	v_cvt_pk_bf16_f32 v224, v224, v225
	v_cvt_pk_bf16_f32 v225, v226, v227
	ds_write_b64 v211, v[224:225] offset:8192
	s_waitcnt lgkmcnt(1)
	v_mfma_f32_32x32x16_bf16 v[2:17], v[126:129], v[130:133], v[2:17]
	v_add_u32_e32 v234, v231, v245
	ds_read_b128 v[34:37], v234 offset:0
	ds_read_b128 v[38:41], v234 offset:16
	ds_read_b128 v[42:45], v234 offset:32
	ds_read_b128 v[46:49], v234 offset:48
	v_add_u32_e32 v232, 0x100, v232
	v_exp_f32_e32 v212, v84
	v_exp_f32_e32 v213, v88
	v_exp_f32_e32 v214, v92
	v_exp_f32_e32 v215, v96
	v_mfma_f32_32x32x16_bf16 v[2:17], v[122:125], v[134:137], v[2:17]
	v_exp_f32_e32 v216, v82
	v_add_f32_e32 v236, 1.0, v212
	v_exp_f32_e32 v217, v86
	v_add_f32_e32 v237, 1.0, v213
	v_exp_f32_e32 v218, v90
	v_add_f32_e32 v238, 1.0, v214
	v_exp_f32_e32 v219, v94
	v_add_f32_e32 v239, 1.0, v215
	v_fma_f32 v240, v212, s12, v235
	v_fma_f32 v241, v213, s12, v235
	v_fma_f32 v242, v214, s12, v235
	v_fma_f32 v243, v215, s12, v235
	v_mfma_f32_32x32x16_bf16 v[2:17], v[118:121], v[138:141], v[2:17]
	v_exp_f32_e32 v220, v83
	v_fmac_f32_e32 v236, v216, v236
	v_exp_f32_e32 v221, v87
	v_fmac_f32_e32 v237, v217, v237
	v_exp_f32_e32 v222, v91
	v_fmac_f32_e32 v238, v218, v238
	v_exp_f32_e32 v223, v95
	v_fmac_f32_e32 v239, v219, v239
	v_mfma_f32_32x32x16_bf16 v[2:17], v[114:117], v[142:145], v[2:17]
	v_rcp_f32_e32 v216, v236
	v_add_f32_e32 v220, 1.0, v220
	v_rcp_f32_e32 v217, v237
	v_add_f32_e32 v221, 1.0, v221
	v_rcp_f32_e32 v218, v238
	v_add_f32_e32 v222, 1.0, v222
	v_rcp_f32_e32 v219, v239
	v_add_f32_e32 v223, 1.0, v223
	v_mfma_f32_32x32x16_bf16 v[2:17], v[110:113], v[146:149], v[2:17]
	v_rcp_f32_e32 v220, v220
	v_mul_f32_e32 v240, v240, v216
	v_rcp_f32_e32 v221, v221
	v_mul_f32_e32 v241, v241, v217
	v_rcp_f32_e32 v222, v222
	v_mul_f32_e32 v242, v242, v218
	v_rcp_f32_e32 v223, v223
	v_mul_f32_e32 v243, v243, v219
	v_mfma_f32_32x32x16_bf16 v[2:17], v[106:109], v[150:153], v[2:17]
	v_exp_f32_e32 v224, v85
	v_fma_f32 v206, v220, v206, v240
	v_exp_f32_e32 v225, v89
	v_fma_f32 v207, v221, v207, v241
	v_exp_f32_e32 v226, v93
	v_fma_f32 v208, v222, v208, v242
	v_exp_f32_e32 v227, v97
	v_fma_f32 v209, v223, v209, v243
	v_mfma_f32_32x32x16_bf16 v[2:17], v[102:105], v[154:157], v[2:17]
	v_exp_f32_e32 v212, v206
	v_add_f32_e32 v224, 1.0, v224
	v_exp_f32_e32 v213, v207
	v_add_f32_e32 v225, 1.0, v225
	v_exp_f32_e32 v214, v208
	v_add_f32_e32 v226, 1.0, v226
	v_exp_f32_e32 v215, v209
	v_add_f32_e32 v227, 1.0, v227
	v_fmac_f32_e32 v224, v224, v212
	v_fmac_f32_e32 v225, v225, v213
	v_fmac_f32_e32 v226, v226, v214
	v_fmac_f32_e32 v227, v227, v215
	v_mfma_f32_32x32x16_bf16 v[2:17], v[98:101], v[158:161], v[2:17]
	v_rcp_f32_e32 v224, v224
	v_rcp_f32_e32 v225, v225
	v_rcp_f32_e32 v226, v226
	v_rcp_f32_e32 v227, v227
	v_fma_f32 v224, -v212, v224, v224
	v_fma_f32 v225, -v213, v225, v225
	v_fma_f32 v226, -v214, v226, v226
	v_fma_f32 v227, -v215, v227, v227
	v_cvt_pk_bf16_f32 v224, v224, v225
	v_cvt_pk_bf16_f32 v225, v226, v227
	ds_write_b64 v211, v[224:225] offset:8200
	s_waitcnt lgkmcnt(0)
	s_barrier
	s_sub_u32 s16, s16, 1
	s_cmp_lg_u32 s16, 0
	s_cbranch_scc1 .Llight_loop
	v_mfma_f32_32x32x16_bf16 v[18:33], v[78:81], v[130:133], v[18:33]
	ds_read_b128 v[162:165], v210 offset:8192
	ds_read_b128 v[166:169], v210 offset:9216
	ds_read_b128 v[82:85], v234 offset:128
	ds_read_b128 v[86:89], v234 offset:144
	ds_read_b128 v[90:93], v234 offset:160
	ds_read_b128 v[94:97], v234 offset:176
	v_exp_f32_e32 v212, v4
	v_exp_f32_e32 v213, v8
	v_exp_f32_e32 v214, v12
	v_exp_f32_e32 v215, v16
	v_mfma_f32_32x32x16_bf16 v[18:33], v[74:77], v[134:137], v[18:33]
	ds_read_b128 v[170:173], v210 offset:10240
	ds_read_b128 v[174:177], v210 offset:11264
	v_exp_f32_e32 v216, v2
	v_add_f32_e32 v236, 1.0, v212
	v_exp_f32_e32 v217, v6
	v_add_f32_e32 v237, 1.0, v213
	v_exp_f32_e32 v218, v10
	v_add_f32_e32 v238, 1.0, v214
	v_exp_f32_e32 v219, v14
	v_add_f32_e32 v239, 1.0, v215
	v_fma_f32 v240, v212, s12, v235
	v_fma_f32 v241, v213, s12, v235
	v_fma_f32 v242, v214, s12, v235
	v_fma_f32 v243, v215, s12, v235
	v_mfma_f32_32x32x16_bf16 v[18:33], v[70:73], v[138:141], v[18:33]
	ds_read_b128 v[178:181], v210 offset:12288
	ds_read_b128 v[182:185], v210 offset:13312
	v_exp_f32_e32 v220, v3
	v_fmac_f32_e32 v236, v216, v236
	v_exp_f32_e32 v221, v7
	v_fmac_f32_e32 v237, v217, v237
	v_exp_f32_e32 v222, v11
	v_fmac_f32_e32 v238, v218, v238
	v_exp_f32_e32 v223, v15
	v_fmac_f32_e32 v239, v219, v239
	v_mfma_f32_32x32x16_bf16 v[18:33], v[66:69], v[142:145], v[18:33]
	ds_read_b128 v[186:189], v210 offset:14336
	ds_read_b128 v[190:193], v210 offset:15360
	v_rcp_f32_e32 v216, v236
	v_add_f32_e32 v220, 1.0, v220
	v_rcp_f32_e32 v217, v237
	v_add_f32_e32 v221, 1.0, v221
	v_rcp_f32_e32 v218, v238
	v_add_f32_e32 v222, 1.0, v222
	v_rcp_f32_e32 v219, v239
	v_add_f32_e32 v223, 1.0, v223
	v_mfma_f32_32x32x16_bf16 v[18:33], v[62:65], v[146:149], v[18:33]
	v_rcp_f32_e32 v220, v220
	v_mul_f32_e32 v240, v240, v216
	v_rcp_f32_e32 v221, v221
	v_mul_f32_e32 v241, v241, v217
	v_rcp_f32_e32 v222, v222
	v_mul_f32_e32 v242, v242, v218
	v_rcp_f32_e32 v223, v223
	v_mul_f32_e32 v243, v243, v219
	v_mfma_f32_32x32x16_bf16 v[18:33], v[58:61], v[150:153], v[18:33]
	v_exp_f32_e32 v224, v5
	v_fma_f32 v194, v220, v194, v240
	v_exp_f32_e32 v225, v9
	v_fma_f32 v195, v221, v195, v241
	v_exp_f32_e32 v226, v13
	v_fma_f32 v196, v222, v196, v242
	v_exp_f32_e32 v227, v17
	v_fma_f32 v197, v223, v197, v243
	v_mfma_f32_32x32x16_bf16 v[18:33], v[54:57], v[154:157], v[18:33]
	v_exp_f32_e32 v212, v194
	v_add_f32_e32 v224, 1.0, v224
	v_exp_f32_e32 v213, v195
	v_add_f32_e32 v225, 1.0, v225
	v_exp_f32_e32 v214, v196
	v_add_f32_e32 v226, 1.0, v226
	v_exp_f32_e32 v215, v197
	v_add_f32_e32 v227, 1.0, v227
	v_fmac_f32_e32 v224, v224, v212
	v_fmac_f32_e32 v225, v225, v213
	v_fmac_f32_e32 v226, v226, v214
	v_fmac_f32_e32 v227, v227, v215
	v_mfma_f32_32x32x16_bf16 v[18:33], v[50:53], v[158:161], v[18:33]
	v_rcp_f32_e32 v224, v224
	v_rcp_f32_e32 v225, v225
	v_rcp_f32_e32 v226, v226
	v_rcp_f32_e32 v227, v227
	v_fma_f32 v224, -v212, v224, v224
	v_fma_f32 v225, -v213, v225, v225
	v_fma_f32 v226, -v214, v226, v226
	v_fma_f32 v227, -v215, v227, v227
	v_cvt_pk_bf16_f32 v224, v224, v225
	v_cvt_pk_bf16_f32 v225, v226, v227
	ds_write_b64 v211, v[224:225] offset:0
	s_waitcnt lgkmcnt(1)
	v_mfma_f32_32x32x16_bf16 v[34:49], v[126:129], v[162:165], v[34:49]
	v_exp_f32_e32 v212, v20
	v_exp_f32_e32 v213, v24
	v_exp_f32_e32 v214, v28
	v_exp_f32_e32 v215, v32
	v_mfma_f32_32x32x16_bf16 v[34:49], v[122:125], v[166:169], v[34:49]
	v_exp_f32_e32 v216, v18
	v_add_f32_e32 v236, 1.0, v212
	v_exp_f32_e32 v217, v22
	v_add_f32_e32 v237, 1.0, v213
	v_exp_f32_e32 v218, v26
	v_add_f32_e32 v238, 1.0, v214
	v_exp_f32_e32 v219, v30
	v_add_f32_e32 v239, 1.0, v215
	v_fma_f32 v240, v212, s12, v235
	v_fma_f32 v241, v213, s12, v235
	v_fma_f32 v242, v214, s12, v235
	v_fma_f32 v243, v215, s12, v235
	v_mfma_f32_32x32x16_bf16 v[34:49], v[118:121], v[170:173], v[34:49]
	v_exp_f32_e32 v220, v19
	v_fmac_f32_e32 v236, v216, v236
	v_exp_f32_e32 v221, v23
	v_fmac_f32_e32 v237, v217, v237
	v_exp_f32_e32 v222, v27
	v_fmac_f32_e32 v238, v218, v238
	v_exp_f32_e32 v223, v31
	v_fmac_f32_e32 v239, v219, v239
	v_mfma_f32_32x32x16_bf16 v[34:49], v[114:117], v[174:177], v[34:49]
	v_rcp_f32_e32 v216, v236
	v_add_f32_e32 v220, 1.0, v220
	v_rcp_f32_e32 v217, v237
	v_add_f32_e32 v221, 1.0, v221
	v_rcp_f32_e32 v218, v238
	v_add_f32_e32 v222, 1.0, v222
	v_rcp_f32_e32 v219, v239
	v_add_f32_e32 v223, 1.0, v223
	v_mfma_f32_32x32x16_bf16 v[34:49], v[110:113], v[178:181], v[34:49]
	v_rcp_f32_e32 v220, v220
	v_mul_f32_e32 v240, v240, v216
	v_rcp_f32_e32 v221, v221
	v_mul_f32_e32 v241, v241, v217
	v_rcp_f32_e32 v222, v222
	v_mul_f32_e32 v242, v242, v218
	v_rcp_f32_e32 v223, v223
	v_mul_f32_e32 v243, v243, v219
	v_mfma_f32_32x32x16_bf16 v[34:49], v[106:109], v[182:185], v[34:49]
	v_exp_f32_e32 v224, v21
	v_fma_f32 v198, v220, v198, v240
	v_exp_f32_e32 v225, v25
	v_fma_f32 v199, v221, v199, v241
	v_exp_f32_e32 v226, v29
	v_fma_f32 v200, v222, v200, v242
	v_exp_f32_e32 v227, v33
	v_fma_f32 v201, v223, v201, v243
	v_mfma_f32_32x32x16_bf16 v[34:49], v[102:105], v[186:189], v[34:49]
	v_exp_f32_e32 v212, v198
	v_add_f32_e32 v224, 1.0, v224
	v_exp_f32_e32 v213, v199
	v_add_f32_e32 v225, 1.0, v225
	v_exp_f32_e32 v214, v200
	v_add_f32_e32 v226, 1.0, v226
	v_exp_f32_e32 v215, v201
	v_add_f32_e32 v227, 1.0, v227
	v_fmac_f32_e32 v224, v224, v212
	v_fmac_f32_e32 v225, v225, v213
	v_fmac_f32_e32 v226, v226, v214
	v_fmac_f32_e32 v227, v227, v215
	v_mfma_f32_32x32x16_bf16 v[34:49], v[98:101], v[190:193], v[34:49]
	v_rcp_f32_e32 v224, v224
	v_rcp_f32_e32 v225, v225
	v_rcp_f32_e32 v226, v226
	v_rcp_f32_e32 v227, v227
	v_fma_f32 v224, -v212, v224, v224
	v_fma_f32 v225, -v213, v225, v225
	v_fma_f32 v226, -v214, v226, v226
	v_fma_f32 v227, -v215, v227, v227
	v_cvt_pk_bf16_f32 v224, v224, v225
	v_cvt_pk_bf16_f32 v225, v226, v227
	ds_write_b64 v211, v[224:225] offset:8
	s_waitcnt lgkmcnt(0)
	s_barrier
	s_bfe_u32 s20, s19, 0x10006
	s_lshl_b32 s21, s20, 7
	s_lshl_b32 s20, s20, 13
	s_add_u32 s20, s20, 0x30000
	s_add_u32 s22, s14, s20
	s_addc_u32 s23, s15, 0
	s_add_u32 s24, s22, 0x1000
	s_addc_u32 s25, s23, 0
	global_load_dwordx4 v[130:133], v210, s[22:23] offset:0
	global_load_dwordx4 v[130:133], v210, s[22:23] offset:1024
	global_load_dwordx4 v[130:133], v210, s[22:23] offset:2048
	global_load_dwordx4 v[130:133], v210, s[22:23] offset:3072
	global_load_dwordx4 v[130:133], v210, s[24:25] offset:0
	global_load_dwordx4 v[130:133], v210, s[24:25] offset:1024
	global_load_dwordx4 v[130:133], v210, s[24:25] offset:2048
	global_load_dwordx4 v[130:133], v210, s[24:25] offset:3072
	v_or_b32_e32 v138, s21, v230
	global_load_dwordx4 v[134:137], v138, s[4:5] offset:0
	global_load_dwordx4 v[134:137], v138, s[4:5] offset:32
	global_load_dwordx4 v[134:137], v138, s[4:5] offset:64
	global_load_dwordx4 v[134:137], v138, s[4:5] offset:96
	global_load_dwordx4 v[134:137], v138, s[6:7] offset:0
	global_load_dwordx4 v[134:137], v138, s[6:7] offset:32
	global_load_dwordx4 v[134:137], v138, s[6:7] offset:64
	global_load_dwordx4 v[134:137], v138, s[6:7] offset:96
	s_load_dword s21, s[8:9], 0x0
	v_mfma_f32_32x32x16_bf16 v[82:97], v[78:81], v[162:165], v[82:97]
	v_exp_f32_e32 v212, v36
	v_exp_f32_e32 v213, v40
	v_exp_f32_e32 v214, v44
	v_exp_f32_e32 v215, v48
	v_mfma_f32_32x32x16_bf16 v[82:97], v[74:77], v[166:169], v[82:97]
	v_exp_f32_e32 v216, v34
	v_add_f32_e32 v236, 1.0, v212
	v_exp_f32_e32 v217, v38
	v_add_f32_e32 v237, 1.0, v213
	v_exp_f32_e32 v218, v42
	v_add_f32_e32 v238, 1.0, v214
	v_exp_f32_e32 v219, v46
	v_add_f32_e32 v239, 1.0, v215
	v_fma_f32 v240, v212, s12, v235
	v_fma_f32 v241, v213, s12, v235
	v_fma_f32 v242, v214, s12, v235
	v_fma_f32 v243, v215, s12, v235
	v_mfma_f32_32x32x16_bf16 v[82:97], v[70:73], v[170:173], v[82:97]
	v_exp_f32_e32 v220, v35
	v_fmac_f32_e32 v236, v216, v236
	v_exp_f32_e32 v221, v39
	v_fmac_f32_e32 v237, v217, v237
	v_exp_f32_e32 v222, v43
	v_fmac_f32_e32 v238, v218, v238
	v_exp_f32_e32 v223, v47
	v_fmac_f32_e32 v239, v219, v239
	v_mfma_f32_32x32x16_bf16 v[82:97], v[66:69], v[174:177], v[82:97]
	v_rcp_f32_e32 v216, v236
	v_add_f32_e32 v220, 1.0, v220
	v_rcp_f32_e32 v217, v237
	v_add_f32_e32 v221, 1.0, v221
	v_rcp_f32_e32 v218, v238
	v_add_f32_e32 v222, 1.0, v222
	v_rcp_f32_e32 v219, v239
	v_add_f32_e32 v223, 1.0, v223
	v_mfma_f32_32x32x16_bf16 v[82:97], v[62:65], v[178:181], v[82:97]
	v_rcp_f32_e32 v220, v220
	v_mul_f32_e32 v240, v240, v216
	v_rcp_f32_e32 v221, v221
	v_mul_f32_e32 v241, v241, v217
	v_rcp_f32_e32 v222, v222
	v_mul_f32_e32 v242, v242, v218
	v_rcp_f32_e32 v223, v223
	v_mul_f32_e32 v243, v243, v219
	v_mfma_f32_32x32x16_bf16 v[82:97], v[58:61], v[182:185], v[82:97]
	v_exp_f32_e32 v224, v37
	v_fma_f32 v202, v220, v202, v240
	v_exp_f32_e32 v225, v41
	v_fma_f32 v203, v221, v203, v241
	v_exp_f32_e32 v226, v45
	v_fma_f32 v204, v222, v204, v242
	v_exp_f32_e32 v227, v49
	v_fma_f32 v205, v223, v205, v243
	v_mfma_f32_32x32x16_bf16 v[82:97], v[54:57], v[186:189], v[82:97]
	v_exp_f32_e32 v212, v202
	v_add_f32_e32 v224, 1.0, v224
	v_exp_f32_e32 v213, v203
	v_add_f32_e32 v225, 1.0, v225
	v_exp_f32_e32 v214, v204
	v_add_f32_e32 v226, 1.0, v226
	v_exp_f32_e32 v215, v205
	v_add_f32_e32 v227, 1.0, v227
	v_fmac_f32_e32 v224, v224, v212
	v_fmac_f32_e32 v225, v225, v213
	v_fmac_f32_e32 v226, v226, v214
	v_fmac_f32_e32 v227, v227, v215
	v_mfma_f32_32x32x16_bf16 v[82:97], v[50:53], v[190:193], v[82:97]
	v_rcp_f32_e32 v224, v224
	v_rcp_f32_e32 v225, v225
	v_rcp_f32_e32 v226, v226
	v_rcp_f32_e32 v227, v227
	v_fma_f32 v224, -v212, v224, v224
	v_fma_f32 v225, -v213, v225, v225
	v_fma_f32 v226, -v214, v226, v226
	v_fma_f32 v227, -v215, v227, v227
	v_cvt_pk_bf16_f32 v224, v224, v225
	v_cvt_pk_bf16_f32 v225, v226, v227
	ds_write_b64 v211, v[224:225] offset:8192
	s_waitcnt lgkmcnt(1)
	v_exp_f32_e32 v212, v84
	v_exp_f32_e32 v213, v88
	v_exp_f32_e32 v214, v92
	v_exp_f32_e32 v215, v96
	v_exp_f32_e32 v216, v82
	v_add_f32_e32 v236, 1.0, v212
	v_exp_f32_e32 v217, v86
	v_add_f32_e32 v237, 1.0, v213
	v_exp_f32_e32 v218, v90
	v_add_f32_e32 v238, 1.0, v214
	v_exp_f32_e32 v219, v94
	v_add_f32_e32 v239, 1.0, v215
	v_fma_f32 v240, v212, s12, v235
	v_fma_f32 v241, v213, s12, v235
	v_fma_f32 v242, v214, s12, v235
	v_fma_f32 v243, v215, s12, v235
	v_exp_f32_e32 v220, v83
	v_fmac_f32_e32 v236, v216, v236
	v_exp_f32_e32 v221, v87
	v_fmac_f32_e32 v237, v217, v237
	v_exp_f32_e32 v222, v91
	v_fmac_f32_e32 v238, v218, v238
	v_exp_f32_e32 v223, v95
	v_fmac_f32_e32 v239, v219, v239
	v_rcp_f32_e32 v216, v236
	v_add_f32_e32 v220, 1.0, v220
	v_rcp_f32_e32 v217, v237
	v_add_f32_e32 v221, 1.0, v221
	v_rcp_f32_e32 v218, v238
	v_add_f32_e32 v222, 1.0, v222
	v_rcp_f32_e32 v219, v239
	v_add_f32_e32 v223, 1.0, v223
	v_rcp_f32_e32 v220, v220
	v_mul_f32_e32 v240, v240, v216
	v_rcp_f32_e32 v221, v221
	v_mul_f32_e32 v241, v241, v217
	v_rcp_f32_e32 v222, v222
	v_mul_f32_e32 v242, v242, v218
	v_rcp_f32_e32 v223, v223
	v_mul_f32_e32 v243, v243, v219
	v_exp_f32_e32 v224, v85
	v_fma_f32 v206, v220, v206, v240
	v_exp_f32_e32 v225, v89
	v_fma_f32 v207, v221, v207, v241
	v_exp_f32_e32 v226, v93
	v_fma_f32 v208, v222, v208, v242
	v_exp_f32_e32 v227, v97
	v_fma_f32 v209, v223, v209, v243
	v_exp_f32_e32 v212, v206
	v_add_f32_e32 v224, 1.0, v224
	v_exp_f32_e32 v213, v207
	v_add_f32_e32 v225, 1.0, v225
	v_exp_f32_e32 v214, v208
	v_add_f32_e32 v226, 1.0, v226
	v_exp_f32_e32 v215, v209
	v_add_f32_e32 v227, 1.0, v227
	v_fmac_f32_e32 v224, v224, v212
	v_fmac_f32_e32 v225, v225, v213
	v_fmac_f32_e32 v226, v226, v214
	v_fmac_f32_e32 v227, v227, v215
	v_rcp_f32_e32 v224, v224
	v_rcp_f32_e32 v225, v225
	v_rcp_f32_e32 v226, v226
	v_rcp_f32_e32 v227, v227
	v_fma_f32 v224, -v212, v224, v224
	v_fma_f32 v225, -v213, v225, v225
	v_fma_f32 v226, -v214, v226, v226
	v_fma_f32 v227, -v215, v227, v227
	v_cvt_pk_bf16_f32 v224, v224, v225
	v_cvt_pk_bf16_f32 v225, v226, v227
	ds_write_b64 v211, v[224:225] offset:8200
	s_waitcnt lgkmcnt(0)
	s_barrier
	s_waitcnt vmcnt(0)
	s_nop 7
	s_nop 7
	s_branch .Lepilogue
